# phase 11: half of the workgroups (blockIdx bit 3) run the S5 scan before the dilated attention so the compute-bound scan overlaps the memory-bound attention of the other half
# baseline (speedup 1.0000x reference)
_Z4mega6Params:
	s_mov_b32 s98, 0
	v_writelane_b32 v253, s98, 60
	s_load_dwordx8 s[72:79], s[0:1], 0x100
	s_load_dwordx4 s[28:31], s[0:1], 0x120
	s_load_dword s34, s[0:1], 0x130
	s_mov_b32 s96, s2
	v_readfirstlane_b32 s2, v0
	v_cmp_gt_u32_e32 vcc, 64, v0
	s_nop 0
	v_writelane_b32 v254, s2, 0
	s_add_u32 s2, s0, 0x130
	s_addc_u32 s3, s1, 0
	v_writelane_b32 v254, s2, 1
	s_nop 1
	v_writelane_b32 v254, s3, 2
	s_and_saveexec_b64 s[4:5], vcc
	v_lshl_add_u32 v1, v0, 2, 0
	v_add_u32_e32 v1, 0x23f00, v1
	v_mov_b32_e32 v2, 0
	ds_write_b32 v1, v2
	s_or_b64 exec, exec, s[4:5]
	s_waitcnt lgkmcnt(0)
	s_add_u32 s2, s28, 0x4000
	s_load_dwordx16 s[8:23], s[0:1], 0x0
	s_addc_u32 s3, s29, 0
	v_writelane_b32 v254, s2, 3
	v_cmp_eq_u32_e32 vcc, 0, v0
	s_waitcnt lgkmcnt(0)
	v_writelane_b32 v254, s3, 4
	s_sub_i32 s2, s31, s30
	s_mov_b32 s3, 0
	v_writelane_b32 v254, s3, 5
	s_cmp_lt_i32 s2, 2
	s_mov_b32 s2, 0
	v_writelane_b32 v254, s2, 6
	s_barrier
	s_cbranch_scc1 .LBB0_7
	s_getreg_b32 s2, hwreg(HW_REG_XCC_ID, 0, 4)
	s_and_b32 s2, s2, 15
	v_writelane_b32 v254, s2, 5
	s_and_saveexec_b64 s[4:5], vcc
	s_cbranch_execz .LBB0_6
	s_mov_b64 s[6:7], exec
	v_mbcnt_lo_u32_b32 v1, s6, 0
	v_mbcnt_hi_u32_b32 v1, s7, v1
	v_cmp_eq_u32_e32 vcc, 0, v1
	s_and_b64 s[2:3], exec, vcc
	s_mov_b64 exec, s[2:3]
	s_cbranch_execz .LBB0_6
	v_readlane_b32 s2, v254, 5
	s_lshl_b32 s2, s2, 8
	s_bcnt1_i32_b64 s3, s[6:7]
	v_mov_b32_e32 v1, s2
	v_mov_b32_e32 v2, s3
	v_readlane_b32 s2, v254, 3
	v_readlane_b32 s3, v254, 4
	s_nop 4
	global_atomic_add v1, v2, s[2:3] offset:1024

.Lp11_redo:
	s_waitcnt vmcnt(0)
	v_lshlrev_b32_e32 v2, 2, v0
	v_lshrrev_b32_e32 v4, 4, v218
	v_and_b32_e32 v2, 12, v2
	v_bfe_u32 v3, v0, 2, 2
	v_or_b32_e32 v5, v2, v3
	v_bitop3_b32 v2, v2, v4, v3 bitop3:0x36
	v_lshlrev_b32_e32 v207, 4, v2
	v_bitop3_b32 v2, v4, v5, 4 bitop3:0x36
	v_lshlrev_b32_e32 v208, 4, v2
	v_bitop3_b32 v2, v4, v5, 8 bitop3:0x36
	s_mov_b32 s0, s96
	v_and_b32_e32 v206, 15, v0
	v_lshlrev_b32_e32 v209, 4, v2
	v_bitop3_b32 v2, v4, v5, 12 bitop3:0x36
	v_writelane_b32 v254, s0, 60
	v_writelane_b32 v253, s26, 22
	v_lshlrev_b32_e32 v152, 8, v206
	v_lshlrev_b32_e32 v210, 4, v2
	v_lshlrev_b32_e32 v150, 2, v4
	v_lshrrev_b32_e32 v151, 1, v218
	v_writelane_b32 v254, s1, 61
	s_cmpk_gt_i32 s96, 0x3ff
	v_mov_b32_e32 v3, 0
	v_writelane_b32 v253, s27, 23
	s_cbranch_scc1 .LBB0_1107
	s_bitcmp1_b32 s96, 3
	s_cbranch_scc0 .Lp11_attn
	v_readlane_b32 s98, v253, 60
	s_cmp_eq_u32 s98, 0
	s_cbranch_scc1 .LBB0_1107
.Lp11_attn:
	v_readlane_b32 s0, v254, 60
	s_add_u32 s3, s28, 0x31400000
	v_readlane_b32 s1, v254, 61
	s_mov_b32 s10, s0
	s_addc_u32 s35, s29, 0
	s_and_b32 s0, s0, 7
	s_lshl_b32 s1, s10, 2
	s_lshl_b32 s0, s0, 2
	s_and_b32 s1, s1, 4
	s_bfe_u32 s2, s10, 0x20001
	s_cmpk_lt_u32 s10, 0x100
	s_cselect_b32 s66, s0, s1
	s_cselect_b32 s2, 0, s2
	s_add_i32 s0, s10, 0xfffffe00
	s_lshr_b32 s8, s0, 7
	s_min_i32 s0, s10, 0x200
	s_bfe_u32 s6, s10, 0x20006
	s_and_b32 s7, s10, 15
	s_ashr_i32 s40, s0, 8
	s_cmpk_lt_i32 s10, 0x200
	s_cselect_b64 s[0:1], -1, 0
	s_and_b64 s[4:5], s[0:1], exec
	s_cselect_b32 s4, 3, 4
	s_cselect_b32 s44, s6, s8
	s_cselect_b32 s41, s2, s7
	s_cselect_b32 s7, s66, 0
	s_lshr_b32 s2, s10, s4
	s_mov_b32 s45, 0
	s_and_b32 s50, s2, 7
	s_lshl_b32 s2, s40, 1
	s_lshl_b64 s[4:5], s[44:45], 12
	s_lshl_b32 s6, 0xc00, s2
	v_lshrrev_b32_e32 v153, 4, v0
	s_cmp_lg_u32 s7, 0
	v_mul_lo_u32 v2, s6, v153
	s_cselect_b64 s[8:9], -1, 0
	s_lshl_b32 s6, s7, 7
	v_lshlrev_b32_e32 v5, 3, v0
	s_addk_i32 s6, 0xff80
	s_or_b32 s11, s4, s41
	s_lshl_b32 s4, s50, 8
	v_and_b32_e32 v154, 0x78, v5
	s_add_u32 s4, s3, s4
	v_or_b32_e32 v2, v2, v154
	s_addc_u32 s10, s35, 0
	s_cmp_eq_u32 s7, 0
	v_lshlrev_b32_e32 v2, 1, v2
	s_cbranch_scc1 .LBB0_1138
	s_mov_b32 s7, s45
	s_lshl_b64 s[12:13], s[6:7], s2
	s_add_u32 s7, s12, s11
	s_addc_u32 s12, s13, s5
	s_mulk_i32 s12, 0x1800
	s_mul_hi_u32 s13, s7, 0x1800
	s_add_i32 s13, s13, s12
	s_mulk_i32 s7, 0x1800
	s_add_u32 s12, s4, s7
	s_addc_u32 s13, s10, s13
	v_lshl_add_u64 v[6:7], s[12:13], 0, v[2:3]
	s_or_b32 s12, s6, 32
	s_mov_b32 s13, s45
	s_lshl_b64 s[12:13], s[12:13], s2
	s_add_u32 s12, s12, s11
	s_addc_u32 s13, s13, s5
	s_mulk_i32 s13, 0x1800
	s_mul_hi_u32 s14, s12, 0x1800
	s_add_i32 s14, s14, s13
	s_mulk_i32 s12, 0x1800
	s_add_u32 s12, s4, s12
	v_add_co_u32_e32 v8, vcc, 0x1000, v6
	s_addc_u32 s13, s10, s14
	s_movk_i32 s7, 0x1000
	v_addc_co_u32_e32 v9, vcc, 0, v7, vcc
	global_load_dwordx4 v[34:37], v[6:7], off offset:2048
	global_load_dwordx4 v[18:21], v[8:9], off
	v_lshl_add_u64 v[6:7], s[12:13], 0, v[2:3]
	v_add_co_u32_e32 v8, vcc, s7, v6
	s_nop 1
	v_addc_co_u32_e32 v9, vcc, 0, v7, vcc
	global_load_dwordx4 v[38:41], v[6:7], off offset:2048
	global_load_dwordx4 v[22:25], v[8:9], off
	v_mov_b32_e32 v42, 0
	s_andn2_b64 vcc, exec, s[8:9]
	s_cbranch_vccnz .LBB0_1139

.LBB0_1107:
	v_readlane_b32 s96, v254, 60
	v_readlane_b32 s26, v253, 22
	s_cmpk_gt_i32 s96, 0xff
	v_readlane_b32 s27, v253, 23
	v_readlane_b32 s97, v254, 61
	s_barrier
	s_cbranch_scc1 .LBB0_1126
	s_bitcmp1_b32 s96, 3
	s_cbranch_scc0 .Lp11_s5
	v_readlane_b32 s98, v253, 60
	s_cmp_lg_u32 s98, 0
	s_cbranch_scc1 .LBB0_1126
.Lp11_s5:
	s_add_u32 s2, s28, 0x37400000
	s_addc_u32 s3, s29, 0
	s_add_u32 s12, s28, 0x3f400000
	v_readlane_b32 s1, v254, 55
	s_addc_u32 s13, s29, 0
	v_lshrrev_b32_e32 v2, 5, v218
	s_lshl_b32 s0, s1, 13
	v_and_b32_e32 v211, 31, v0
	s_add_i32 s4, s0, 0
	s_lshl_b32 s0, s1, 7
	v_lshlrev_b32_e32 v4, 6, v2
	v_or3_b32 v4, s0, v4, v211
	v_lshlrev_b32_e32 v6, 3, v4
	v_lshlrev_b32_e32 v4, 2, v211
	v_readlane_b32 s52, v254, 39
	v_lshl_or_b32 v212, s1, 1, v2
	v_lshlrev_b32_e32 v2, 12, v2
	v_and_b32_e32 v5, 0x70, v4
	v_readlane_b32 s53, v254, 40
	v_readlane_b32 s54, v254, 41
	v_readlane_b32 s55, v254, 42
	v_readlane_b32 s56, v254, 43
	v_readlane_b32 s57, v254, 44
	v_readlane_b32 s58, v254, 45
	v_readlane_b32 s59, v254, 46
	v_readlane_b32 s60, v254, 47
	v_readlane_b32 s61, v254, 48
	v_readlane_b32 s62, v254, 49
	v_readlane_b32 s63, v254, 50
	v_add3_u32 v7, s4, v5, v2
	v_mov_b32_e32 v5, 0x70
	s_movk_i32 s6, 0x50
	v_readlane_b32 s64, v254, 51
	v_readlane_b32 s65, v254, 52
	v_readlane_b32 s66, v254, 53
	v_readlane_b32 s67, v254, 54
	s_mov_b64 s[52:53], s[56:57]
	v_lshrrev_b32_e32 v3, 2, v0
	v_mov_b32_e32 v173, 0
	s_movk_i32 s5, 0x70
	v_bitop3_b32 v11, v4, s6, v5 bitop3:0x6c
	s_movk_i32 s6, 0x60
	v_and_b32_e32 v172, 32, v218
	s_mov_b64 s[54:55], s[58:59]
	s_mov_b64 s[56:57], s[60:61]
	s_mov_b64 s[58:59], s[62:63]
	s_mov_b64 s[60:61], s[64:65]
	s_lshl_b32 s16, s1, 9
	v_and_b32_e32 v8, 12, v4
	v_bitop3_b32 v9, v4, 64, v5 bitop3:0x6c
	v_bitop3_b32 v10, v4, 16, v5 bitop3:0x6c
	v_bitop3_b32 v12, v4, 32, v5 bitop3:0x6c
	v_bitop3_b32 v13, v4, s6, v5 bitop3:0x6c
	v_bitop3_b32 v5, v4, 48, v5 bitop3:0x6c
	v_bitop3_b32 v4, v4, s5, v4 bitop3:0xc
	v_lshl_add_u64 v[180:181], s[58:59], 0, v[172:173]
	v_lshl_add_u64 v[182:183], s[60:61], 0, v[172:173]
	v_lshlrev_b32_e32 v172, 2, v150
	v_and_b32_e32 v3, 8, v3
	v_add3_u32 v9, s4, v9, v2
	v_add3_u32 v10, s4, v10, v2
	v_add3_u32 v11, s4, v11, v2
	v_add3_u32 v12, s4, v12, v2
	v_add3_u32 v13, s4, v13, v2
	v_add3_u32 v14, s4, v5, v2
	v_add3_u32 v15, s4, v4, v2
	s_ashr_i32 s17, s16, 31
	v_lshl_add_u64 v[184:185], s[38:39], 0, v[172:173]
	v_lshlrev_b32_e32 v2, 6, v0
	v_lshlrev_b32_e32 v172, 1, v3
	v_lshl_add_u32 v3, v211, 3, 0
	v_mov_b32_e32 v177, s17
	v_or_b32_e32 v176, s16, v206
	v_and_b32_e32 v2, 0x100, v2
	v_add_u32_e32 v214, 0x10100, v3
	v_and_b32_e32 v3, 48, v0
	v_or_b32_e32 v2, s16, v2
	v_lshlrev_b64 v[4:5], 11, v[176:177]
	v_lshrrev_b32_e32 v3, 1, v3
	v_ashrrev_i32_e32 v187, 31, v2
	v_or_b32_e32 v4, v4, v3
	v_lshlrev_b32_e32 v3, 10, v218
	v_and_or_b32 v2, v0, 3, v2
	v_lshl_add_u64 v[190:191], s[28:29], 0, v[4:5]
	v_and_b32_e32 v4, 0x6000, v3
	v_mov_b32_e32 v3, v187
	v_lshrrev_b32_e32 v5, 1, v0
	v_and_or_b32 v186, v151, 12, v2
	v_lshlrev_b64 v[2:3], 11, v[2:3]
	v_and_b32_e32 v5, 16, v5
	v_or3_b32 v2, v2, v4, v5
	s_or_b32 s18, s16, 0x100
	v_lshl_add_u64 v[192:193], s[28:29], 0, v[2:3]
	v_lshlrev_b32_e32 v170, 1, v150
	v_mov_b32_e32 v171, v173
	s_ashr_i32 s19, s18, 31
	s_mov_b64 s[62:63], s[66:67]
	v_lshl_or_b32 v16, v206, 6, v150
	v_add_u32_e32 v2, 0, v6
	s_mov_b32 s15, 0
	v_lshl_add_u64 v[174:175], s[2:3], 0, v[170:171]
	v_cmp_ne_u32_e64 s[0:1], 0, v212
	v_add_u32_e32 v213, s4, v152
	v_mov_b32_e32 v179, s19
	v_or_b32_e32 v178, s18, v206
	v_lshl_add_u64 v[188:189], s[2:3], 0, v[172:173]
	s_mov_b32 s3, 0x3fb8aa3b
	s_brev_b32 s22, 18
	s_mov_b32 s23, 0xfe5163ab
	s_mov_b32 s24, 0x3c439041
	s_mov_b32 s25, 0xdb629599
	s_mov_b32 s35, 0xf534ddc0
	s_mov_b32 s38, 0xfc2757d1
	s_mov_b32 s39, 0x4e441529
	s_mov_b32 s40, 0xa2f9836e
	s_mov_b32 s41, 0x3fc90fda
	s_mov_b32 s44, 0x3f22f983
	s_mov_b32 s45, 0xbfc90fda
	s_mov_b32 s50, 0xc2ce8ed0
	s_mov_b32 s51, 0x42b17218
	v_mov_b32_e32 v215, 0x3c0881c4
	v_mov_b32_e32 v216, 0xbab64f3b
	s_brev_b32 s52, 1
	s_movk_i32 s53, 0x1f8
	v_lshlrev_b32_e32 v217, 2, v16
	v_add_u32_e32 v219, 0x10000, v2
	s_mov_b32 s54, 0x3f420000
	s_mov_b32 s55, 0x3f4a0000
	s_mov_b32 s56, 0x3f428000
	s_mov_b32 s57, 0x3f4a8000
	s_mov_b32 s58, 0x3f430000
	s_mov_b32 s59, 0x3f4b0000
	s_mov_b32 s60, 0x3f438000
	s_mov_b32 s61, 0x3f4b8000
	v_not_b32_e32 v220, 63
	v_not_b32_e32 v221, 31
	v_mov_b32_e32 v222, 0x7f800000
	v_mov_b32_e32 v223, 0x7fc00000
	v_mov_b32_e32 v224, 0x800
	v_add_u32_e32 v225, v7, v8
	v_add_u32_e32 v226, v9, v8
	v_add_u32_e32 v227, v10, v8
	v_add_u32_e32 v228, v11, v8
	v_add_u32_e32 v229, v12, v8
	v_add_u32_e32 v230, v13, v8
	v_add_u32_e32 v231, v14, v8
	v_add_u32_e32 v232, v15, v8
	s_mov_b32 s62, s96
	s_mov_b32 s63, s96

.LBB0_1126:
	v_readlane_b32 s98, v254, 60
	s_bitcmp1_b32 s98, 3
	s_cbranch_scc0 .Lp11_done
	v_readlane_b32 s98, v253, 60
	s_cmp_lg_u32 s98, 0
	s_cbranch_scc1 .Lp11_done
	s_mov_b32 s98, 1
	v_writelane_b32 v253, s98, 60
	v_readlane_b32 s96, v254, 60
	v_readlane_b32 s1, v254, 61
	v_readlane_b32 s26, v253, 22
	v_readlane_b32 s27, v253, 23
	s_branch .Lp11_redo
